# XCD-local unit order for the grouped GEMMs: 4 column tiles of a row tile on one XCD
# baseline (speedup 1.0000x reference)
; __global__ void __launch_bounds__(NTHR, 2) mega_fwd(Args a) {
;     ...
;         xcd_barrier(bar);
;     }
;     fin_combine(a, NL - 1);
.LBB0_103:
	s_or_b64 exec, exec, s[36:37]
	s_nop 1
	v_readlane_b32 s61, v254, 61
	s_nop 1
	s_add_u32 vcc_lo, s61, s77
	s_nop 1
	v_writelane_b32 v253, vcc_lo, 31
	s_nop 1
	v_readlane_b32 s4, v254, 16
	v_readlane_b32 s5, v254, 17
	s_mov_b32 s62, 1
	s_mov_b64 s[44:45], 0
	s_and_b64 vcc, exec, s[4:5]
	s_waitcnt lgkmcnt(0)
	s_barrier
	s_cbranch_vccz .LBB0_104
	s_getpc_b64 s[98:99]

; #define LAS __attribute__((address_space(3)))
; __device__ __forceinline__ int opaque_tid() { int t = threadIdx.x; asm volatile("" : "+v"(t)); return t; }
; __device__ __forceinline__ void seg_to_lds(const Args& a, LAS unsigned char* lds, int layer) {
;     LAS int* seg = (LAS int*)(lds + SEG_OFF);
;     const int t = opaque_tid();
;     if (t < 16) {
;         unsigned* cnt = (unsigned*)(a.ws + WS_CTL) + CW_CNT + layer * 16 * 64;
;         const int c = (int)__hip_atomic_load(cnt + t * 64, __ATOMIC_RELAXED, __HIP_MEMORY_SCOPE_AGENT);
;         const int pad = (c + 255) & ~255;
;         int incl = pad;
; #pragma unroll
;         for (int o2 = 1; o2 < 16; o2 <<= 1) { const int u2 = __shfl_up(incl, o2); if (t >= o2) incl += u2; }
;         seg[t] = c; seg[16 + t] = incl - pad;
;         if (t == 15) seg[32] = incl;
;     }
;     __syncthreads();
; }
; __device__ __forceinline__ void gu_mfma(const Args& a, LAS unsigned char* lds, int layer) {
;     seg_to_lds(a, lds, layer);
;     const LAS int* seg = (const LAS int*)(lds + SEG_OFF);
;     pg8::GroupedOrder So{(const char*)(a.ws + WS_HS), (const char*)(a.ws + WS_WGU + (size_t)layer * NE * 1024 * D * 2), seg, 4, (int)gridDim.x, (int)blockIdx.x, (size_t)D * 2, (size_t)1024 * D * 2, (size_t)256 * D * 2};
;     EpiGU E{(bf16_t*)(a.ws + WS_HID), seg};
;     pg8::gemm_phase_gather<EpiGU, pg8::GroupedOrder>(lds, D, So, E, (const char*)(a.ws + WS_ACT), (const int*)(a.ws + WS_LIST), seg);
.LBB0_898:
	s_or_b64 exec, exec, s[36:37]
	s_nop 1
	v_writelane_b32 v254, s61, 61
	s_nop 1
	s_and_b32 vcc_lo, s61, 7
	s_lshl_b32 vcc_lo, vcc_lo, 2
	s_lshr_b32 vcc_hi, s61, 3
	s_and_b32 vcc_hi, vcc_hi, 3
	s_or_b32 vcc_lo, vcc_lo, vcc_hi
	s_andn2_b32 s61, s61, 31
	s_or_b32 s61, s61, vcc_lo
	s_add_u32 vcc_lo, s61, s77
	s_nop 1
	v_writelane_b32 v253, vcc_lo, 31
	s_nop 1
	v_mov_b32_e32 v1, v0
	s_waitcnt lgkmcnt(0)
	s_barrier
	s_nop 0
	v_cmp_gt_i32_e32 vcc, 16, v1
	s_and_saveexec_b64 s[4:5], vcc
	s_cbranch_execz .LBB0_901
	v_lshlrev_b32_e32 v2, 6, v1
	v_readlane_b32 s6, v254, 22
	v_ashrrev_i32_e32 v3, 31, v2
	v_readlane_b32 s7, v254, 23
	v_cmp_lt_i32_e32 vcc, v235, v240
	s_nop 0
	v_lshl_add_u64 v[2:3], v[2:3], 2, s[6:7]
	global_load_dword v3, v[2:3], off sc1
	s_waitcnt vmcnt(0)
	v_add_u32_e32 v2, 0xff, v3
	v_and_b32_e32 v4, 0xffffff00, v2
	v_cndmask_b32_e32 v2, v235, v199, vcc
	v_lshlrev_b32_e32 v2, 2, v2
	ds_bpermute_b32 v2, v2, v4
	v_cmp_lt_i32_e32 vcc, 0, v1
	s_waitcnt lgkmcnt(0)
	s_nop 0
	v_cndmask_b32_e32 v2, 0, v2, vcc
	v_cmp_lt_i32_e32 vcc, v233, v240
	v_add_u32_e32 v2, v4, v2
	s_nop 0
	v_cndmask_b32_e32 v5, v233, v199, vcc
	v_lshlrev_b32_e32 v5, 2, v5
	ds_bpermute_b32 v5, v5, v2
	v_cmp_lt_i32_e32 vcc, 1, v1
	s_waitcnt lgkmcnt(0)
	s_nop 0
	v_cndmask_b32_e32 v5, 0, v5, vcc
	v_cmp_lt_i32_e32 vcc, v243, v240
	v_add_u32_e32 v2, v2, v5
	s_nop 0
	v_cndmask_b32_e32 v5, v243, v199, vcc
	v_lshlrev_b32_e32 v5, 2, v5
	ds_bpermute_b32 v5, v5, v2
	v_cmp_lt_i32_e32 vcc, 3, v1
	s_waitcnt lgkmcnt(0)
	s_nop 0
	v_cndmask_b32_e32 v5, 0, v5, vcc
	v_cmp_lt_i32_e32 vcc, v203, v240
	v_add_u32_e32 v2, v2, v5
	s_nop 0
	v_cndmask_b32_e32 v5, v203, v199, vcc
	v_lshlrev_b32_e32 v5, 2, v5
	ds_bpermute_b32 v5, v5, v2
	v_cmp_lt_i32_e32 vcc, 7, v1
	s_waitcnt lgkmcnt(0)
	s_nop 0
	v_cndmask_b32_e32 v5, 0, v5, vcc
	v_add_u32_e32 v2, v2, v5
	v_lshl_add_u32 v5, v1, 2, 0
	v_add_u32_e32 v5, 0x21e00, v5
	v_sub_u32_e32 v4, v2, v4
	v_cmp_eq_u32_e32 vcc, 15, v1
	ds_write2_b32 v5, v3, v4 offset1:16
	s_and_b64 exec, exec, vcc
	s_cbranch_execz .LBB0_901
	v_readlane_b32 s2, v253, 58
	s_nop 1
	v_mov_b32_e32 v1, s2
	ds_write_b32 v1, v2
